# speedup vs baseline: 1.0612x; 1.0075x over previous
_Z10agg_kernelPKDF16_PKiS2_S2_PKfS2_PDF16_Pfi:
	s_load_dwordx8 s[12:19], s[0:1], 0x0
	s_lshl_b32 s4, s2, 1
	s_ashr_i32 s5, s4, 31
	s_lshl_b64 s[4:5], s[4:5], 2
	v_and_b32_e32 v1, 63, v0
	s_waitcnt lgkmcnt(0)
	s_add_u32 s20, s16, s4
	s_addc_u32 s21, s17, s5
	s_load_dwordx2 s[16:17], s[20:21], 0x0
	s_load_dwordx8 s[4:11], s[0:1], 0x20
	v_readfirstlane_b32 s3, v0
	v_lshlrev_b32_e32 v2, 2, v1
	s_lshr_b32 s3, s3, 6
	s_waitcnt lgkmcnt(0)
	s_ashr_i32 s21, s16, 31
	s_mov_b32 s20, s16
	global_load_dword v3, v2, s[6:7]
	global_load_dword v4, v2, s[6:7] offset:256
	global_load_dword v6, v2, s[6:7] offset:512
	global_load_dword v5, v2, s[6:7] offset:768
	s_lshl_b64 s[6:7], s[20:21], 2
	s_add_u32 s6, s14, s6
	s_addc_u32 s7, s15, s7
	s_add_i32 s21, s17, 15
	s_ashr_i32 s21, s21, 4
	s_max_i32 s20, s21, 1
	s_add_i32 s20, s20, -1
	s_min_u32 s14, s3, s20
	s_bfe_u32 s44, s2, 0x10002
	s_mul_i32 s45, s44, s20
	s_lshl_b32 s44, s44, 1
	s_sub_i32 s44, 1, s44
	s_mul_i32 s14, s14, s44
	s_add_i32 s14, s14, s45
	s_lshl_b32 s30, s14, 4
	v_mov_b32_e32 v59, 0x30e0000
	v_bfe_u32 v2, v0, 4, 2
	v_lshlrev_b32_e32 v7, 2, v0
	s_lshl_b32 s14, s14, 6
	v_and_or_b32 v18, v7, 12, v2
	s_add_u32 s14, s6, s14
	s_addc_u32 s15, s7, 0
	v_lshlrev_b32_e32 v2, 2, v18
	global_load_dword v2, v2, s[14:15] nt
	v_lshlrev_b32_e32 v20, 2, v18
	v_mov_b32_e32 v8, 0
	v_mov_b32_e32 v9, 0
	v_mov_b32_e32 v10, 0
	v_mov_b32_e32 v11, 0
	v_lshlrev_b32_e32 v12, 4, v0
	v_add_u32_e32 v13, 0x10000, v12
	ds_write_b128 v12, v[8:11]
	ds_write_b128 v12, v[8:11] offset:16384
	ds_write_b128 v12, v[8:11] offset:32768
	ds_write_b128 v12, v[8:11] offset:49152
	ds_write_b128 v13, v[8:11]
	ds_write_b128 v13, v[8:11] offset:16384
	ds_write_b128 v13, v[8:11] offset:32768
	v_cmp_gt_u32_e32 vcc, 0x28c, v0
	s_and_saveexec_b64 s[14:15], vcc
	ds_write_b128 v13, v[8:11] offset:49152
	s_or_b64 exec, exec, s[14:15]
	s_waitcnt vmcnt(2)
	v_max3_i32 v3, v3, v4, v6
	v_mbcnt_lo_u32_b32 v4, -1, 0
	v_mbcnt_hi_u32_b32 v4, -1, v4
	v_and_b32_e32 v25, 64, v4
	s_waitcnt vmcnt(1)
	v_max3_i32 v3, v3, v5, 0
	v_add_u32_e32 v5, 64, v25
	v_xor_b32_e32 v6, 1, v4
	v_cmp_lt_i32_e32 vcc, v6, v5
	s_load_dword s16, s[0:1], 0x40
	s_mul_i32 s14, s2, 0x187
	v_cndmask_b32_e32 v6, v4, v6, vcc
	v_lshlrev_b32_e32 v6, 2, v6
	ds_bpermute_b32 v6, v6, v3
	s_waitcnt lgkmcnt(0)
	s_sub_i32 s15, s16, s14
	s_movk_i32 s0, 0x73
	s_cmp_gt_i32 s21, s3
	s_cselect_b64 s[22:23], -1, 0
	v_max_i32_e32 v3, v3, v6
	v_xor_b32_e32 v6, 2, v4
	v_cmp_lt_i32_e32 vcc, v6, v5
	v_mov_b32_e32 v29, 0
	v_mov_b32_e32 v27, 0
	v_cndmask_b32_e32 v6, v4, v6, vcc
	v_lshlrev_b32_e32 v6, 2, v6
	ds_bpermute_b32 v6, v6, v3
	v_mov_b32_e32 v28, 0
	v_mov_b32_e32 v26, 0
	v_mov_b32_e32 v21, 0
	s_waitcnt vmcnt(0)
	v_add_u32_e32 v33, s30, v18
	v_cmp_gt_i32_e64 s[28:29], s17, v33
	s_nop 1
	v_cndmask_b32_e64 v2, v59, v2, s[28:29]
	s_nop 1
	v_mov_b32_dpp v29, v2 row_newbcast:0 row_mask:0xf bank_mask:0xf
	s_waitcnt lgkmcnt(0)
	v_max_i32_e32 v3, v3, v6
	v_xor_b32_e32 v6, 4, v4
	v_cmp_lt_i32_e32 vcc, v6, v5
	v_mov_b32_dpp v27, v2 row_newbcast:1 row_mask:0xf bank_mask:0xf
	v_mov_b32_dpp v28, v2 row_newbcast:2 row_mask:0xf bank_mask:0xf
	v_cndmask_b32_e32 v6, v4, v6, vcc
	v_lshlrev_b32_e32 v6, 2, v6
	ds_bpermute_b32 v6, v6, v3
	v_mov_b32_dpp v26, v2 row_newbcast:3 row_mask:0xf bank_mask:0xf
	s_waitcnt lgkmcnt(0)
	s_barrier
	v_max_i32_e32 v3, v3, v6
	v_xor_b32_e32 v6, 8, v4
	v_cmp_lt_i32_e32 vcc, v6, v5
	s_nop 1
	v_cndmask_b32_e32 v6, v4, v6, vcc
	v_lshlrev_b32_e32 v60, 2, v6
	ds_bpermute_b32 v6, v60, v3
	s_waitcnt lgkmcnt(0)
	v_max_i32_e32 v3, v3, v6
	v_xor_b32_e32 v6, 16, v4
	v_cmp_lt_i32_e32 vcc, v6, v5
	s_nop 1
	v_cndmask_b32_e32 v6, v4, v6, vcc
	v_lshlrev_b32_e32 v61, 2, v6
	ds_bpermute_b32 v6, v61, v3
	s_waitcnt lgkmcnt(0)
	v_max_i32_e32 v3, v3, v6
	v_xor_b32_e32 v6, 32, v4
	v_cmp_lt_i32_e32 vcc, v6, v5
	v_and_b32_e32 v5, 15, v0
	v_lshlrev_b32_e32 v24, 4, v5
	v_cndmask_b32_e32 v4, v4, v6, vcc
	v_lshlrev_b32_e32 v66, 2, v4
	ds_bpermute_b32 v4, v66, v3
	v_lshlrev_b32_e32 v23, 2, v5
	s_waitcnt lgkmcnt(0)
	v_max_i32_e32 v3, v3, v4
	v_lshrrev_b32_e32 v3, 23, v3
	v_mov_b32_e32 v4, 0x8b
	v_med3_u32 v3, v3, s0, v4
	s_sub_i32 s0, s21, s3
	s_add_i32 s0, s0, 15
	s_cmp_gt_u32 s0, 15
	s_cselect_b64 s[24:25], -1, 0
	v_lshlrev_b32_e32 v19, 23, v3
	s_and_b64 s[22:23], s[22:23], s[24:25]
	v_sub_u32_e32 v22, 0x84800000, v19
	s_and_b64 vcc, exec, s[22:23]
	s_cbranch_vccz .LBB2_5
	s_lshr_b32 s21, s0, 4
	s_mov_b32 s1, 0
	s_mov_b32 s22, 0x1ffff00
	s_mov_b32 s23, 0x4b400000
	v_lshl_add_u64 v[20:21], s[6:7], 0, v[20:21]
	s_add_i32 s0, s3, 16
	s_mov_b32 s24, s0
	s_min_i32 s24, s24, s20
	s_mul_i32 s24, s24, s44
	s_add_i32 s24, s24, s45
	s_lshl_b32 s24, s24, 4
	s_ashr_i32 s25, s24, 31
	v_lshl_add_u64 v[32:33], s[24:25], 2, v[20:21]
	global_load_dword v30, v[32:33], off nt
	v_lshlrev_b32_e32 v35, 8, v29
	v_and_or_b32 v35, v35, s22, v24
	global_load_dwordx4 v[2:5], v35, s[12:13]
	v_lshlrev_b32_e32 v35, 8, v27
	v_and_or_b32 v35, v35, s22, v24
	global_load_dwordx4 v[6:9], v35, s[12:13]
	v_lshlrev_b32_e32 v35, 8, v28
	v_and_or_b32 v35, v35, s22, v24
	global_load_dwordx4 v[10:13], v35, s[12:13]
	v_lshlrev_b32_e32 v35, 8, v26
	v_and_or_b32 v35, v35, s22, v24
	global_load_dwordx4 v[14:17], v35, s[12:13]
